# speedup vs baseline: 1.0069x; 1.0069x over previous
.LBB1_47:
	s_mul_i32 s2, s33, 0x1388
	v_mov_b32_e32 v4, 0
	v_add_u32_e32 v2, s2, v0
	v_mov_b32_e32 v3, v4
	v_or_b32_e32 v33, 0x400, v0
	s_waitcnt lgkmcnt(0)
	v_lshl_add_u64 v[6:7], v[2:3], 3, s[38:39]
	v_add_u32_e32 v2, s2, v33
	v_or_b32_e32 v31, 0x800, v0
	v_lshl_add_u64 v[8:9], v[2:3], 3, s[38:39]
	v_add_u32_e32 v2, s2, v31
	v_or_b32_e32 v29, 0xc00, v0
	v_lshl_add_u64 v[10:11], v[2:3], 3, s[38:39]
	v_add_u32_e32 v2, s2, v29
	v_lshl_add_u64 v[12:13], v[2:3], 3, s[38:39]
	global_load_dwordx2 v[2:3], v[6:7], off
	global_load_dwordx2 v[24:25], v[8:9], off
	global_load_dwordx2 v[22:23], v[10:11], off
	global_load_dwordx2 v[20:21], v[12:13], off
	s_movk_i32 s0, 0x1388
	v_or_b32_e32 v28, 0x1000, v0
	v_cmp_gt_u32_e32 vcc, s0, v28
	v_mov_b32_e32 v19, 64
	v_mov_b32_e32 v18, 0
	s_and_saveexec_b64 s[0:1], vcc
	s_cbranch_execz .LBB1_49
	v_add_u32_e32 v6, s2, v28
	v_mov_b32_e32 v7, 0
	v_lshl_add_u64 v[6:7], v[6:7], 3, s[38:39]
	global_load_dwordx2 v[18:19], v[6:7], off
.LBB1_49:
	s_or_b64 exec, exec, s[0:1]
	s_mov_b32 s18, 0
	v_lshlrev_b32_e32 v1, 1, v0
	v_xor_b32_e32 v8, 0x7fe, v1
	v_lshlrev_b32_e32 v9, 2, v8
	v_mov_b32_e32 v5, v4
	v_cmp_gt_u32_e32 vcc, 8, v0
	v_lshlrev_b32_e32 v27, 2, v0
	ds_write_b64 v9, v[4:5]
	s_and_saveexec_b64 s[0:1], vcc
	v_mov_b32_e32 v1, 0
	ds_write_b32 v27, v1 offset:8192
	s_or_b64 exec, exec, s[0:1]
	v_cmp_gt_u32_e64 s[0:1], 17, v0
	s_and_saveexec_b64 s[2:3], s[0:1]
	v_mov_b32_e32 v1, 0
	ds_write_b32 v27, v1 offset:48288
	s_or_b64 exec, exec, s[2:3]
	v_lshrrev_b32_e32 v34, 6, v0
	v_and_b32_e32 v1, 63, v0
	s_waitcnt lgkmcnt(0)
	s_barrier
	v_cmp_gt_u32_e32 vcc, 17, v1
	v_cmp_gt_u32_e64 s[2:3], v1, v34
	s_and_b64 s[16:17], vcc, s[2:3]
	s_waitcnt vmcnt(3)
	v_cmp_ne_u32_e64 s[14:15], 0, v2
	s_waitcnt vmcnt(2)
	v_cmp_ne_u32_e64 s[12:13], 0, v24
	s_waitcnt vmcnt(1)
	v_cmp_ne_u32_e64 s[10:11], 0, v22
	s_waitcnt vmcnt(0)
	v_cmp_ne_u32_e64 s[6:7], 0, v20
	v_cmp_ne_u32_e64 s[4:5], 0, v18
	v_mov_b32_e32 v4, 0
	v_lshlrev_b32_e32 v30, 2, v34
	v_lshlrev_b32_e32 v15, 2, v1
	v_mov_b32_e32 v16, 1
	s_movk_i32 s22, 0x12c
	v_mov_b32_e32 v5, v4
	s_branch .LBB1_56

.LBB1_56:
	s_waitcnt lgkmcnt(0)
	s_max_u32 s20, s18, 0x3c000000
	s_min_u32 s2, s20, 1.0
	s_add_i32 s2, s2, 0xc27fffff
	s_cmp_lt_u32 s2, 0x2000000
	s_cselect_b32 s21, 14, 15
	v_sub_u32_e64 v6, v2, s20 clamp
	v_lshrrev_b32_e32 v6, s21, v6
	v_min_u32_e32 v14, 0x7ff, v6
	s_and_saveexec_b64 s[2:3], s[14:15]
	v_lshlrev_b32_e32 v6, 2, v14
	ds_add_u32 v6, v16
	s_or_b64 exec, exec, s[2:3]
	v_sub_u32_e64 v6, v24, s20 clamp
	v_lshrrev_b32_e32 v6, s21, v6
	v_min_u32_e32 v13, 0x7ff, v6
	s_and_saveexec_b64 s[2:3], s[12:13]
	v_lshlrev_b32_e32 v6, 2, v13
	ds_add_u32 v6, v16
	s_or_b64 exec, exec, s[2:3]
	v_sub_u32_e64 v6, v22, s20 clamp
	v_lshrrev_b32_e32 v6, s21, v6
	v_min_u32_e32 v12, 0x7ff, v6
	s_and_saveexec_b64 s[2:3], s[10:11]
	v_lshlrev_b32_e32 v6, 2, v12
	ds_add_u32 v6, v16
	s_or_b64 exec, exec, s[2:3]
	v_sub_u32_e64 v6, v20, s20 clamp
	v_lshrrev_b32_e32 v6, s21, v6
	v_min_u32_e32 v11, 0x7ff, v6
	s_and_saveexec_b64 s[2:3], s[6:7]
	v_lshlrev_b32_e32 v6, 2, v11
	ds_add_u32 v6, v16
	s_or_b64 exec, exec, s[2:3]
	v_sub_u32_e64 v6, v18, s20 clamp
	v_lshrrev_b32_e32 v6, s21, v6
	v_min_u32_e32 v10, 0x7ff, v6
	s_and_saveexec_b64 s[2:3], s[4:5]
	v_lshlrev_b32_e32 v6, 2, v10
	ds_add_u32 v6, v16
	s_or_b64 exec, exec, s[2:3]
	s_waitcnt lgkmcnt(0)
	s_barrier
	ds_read_b64 v[6:7], v9
	s_waitcnt lgkmcnt(0)
	v_add_u32_e32 v17, v7, v6
	s_nop 1
	v_add_u32_dpp v26, v17, v17 row_shr:1 row_mask:0xf bank_mask:0xf bound_ctrl:1
	s_nop 1
	v_add_u32_dpp v26, v26, v26 row_shr:2 row_mask:0xf bank_mask:0xf bound_ctrl:1
	s_nop 1
	v_add_u32_dpp v26, v26, v26 row_shr:4 row_mask:0xf bank_mask:0xf bound_ctrl:1
	s_nop 1
	v_add_u32_dpp v26, v26, v26 row_shr:8 row_mask:0xf bank_mask:0xf bound_ctrl:1
	s_nop 1
	v_add_u32_dpp v26, v26, v26 row_bcast:15 row_mask:0xa bank_mask:0xf
	s_nop 1
	v_add_u32_dpp v26, v26, v26 row_bcast:31 row_mask:0xc bank_mask:0xf
	s_nop 0
	v_readlane_b32 s8, v26, 63
	s_and_saveexec_b64 s[2:3], s[16:17]
	s_nop 0
	v_mov_b32_e32 v32, s8
	ds_add_u32 v15, v32 offset:48288
	s_or_b64 exec, exec, s[2:3]
	s_waitcnt lgkmcnt(0)
	s_barrier
	ds_read_b32 v32, v4 offset:48352
	ds_read_b32 v35, v30 offset:48288
	s_cmp_eq_u32 s18, 0
	s_cselect_b64 s[8:9], -1, 0
	s_waitcnt lgkmcnt(1)
	v_cmp_lt_i32_e64 s[2:3], s22, v32
	s_or_b64 s[8:9], s[8:9], s[2:3]
	s_and_b64 vcc, exec, s[8:9]
	s_cbranch_vccnz .LBB1_55
	s_waitcnt lgkmcnt(0)
	s_barrier
	ds_write_b64 v9, v[4:5]
	s_and_saveexec_b64 s[18:19], s[0:1]
	s_cbranch_execz .LBB1_54
	ds_write_b32 v27, v4 offset:48288
	s_branch .LBB1_54
